# nt hint also on the combine phase's once-read loads (token positions, expert output rows, residual) and the final RMSNorm's row loads, on top of the prologue nt loads
# speedup vs baseline: 1.0078x; 1.0011x over previous
.LBB0_1685:
	global_load_dwordx4 v[2:5], v11, s[8:9] nt
	v_add_co_u32_e32 v20, vcc, -0.5, v14
	v_lshl_add_u64 v[18:19], v[14:15], 0, s[14:15]
	s_nop 0
	v_addc_co_u32_e32 v21, vcc, -1, v15, vcc
	global_load_dwordx4 v[28:31], v[20:21], off nt
	global_load_dwordx4 v[32:35], v[18:19], off offset:16 nt
	v_mov_b32_e32 v6, v11
	v_mov_b32_e32 v7, v11
	v_mov_b32_e32 v8, v11
	v_mov_b32_e32 v9, v11
	s_add_i32 s0, s0, s50
	s_add_u32 s8, s8, s10
	s_addc_u32 s9, s9, s11
	s_cmp_gt_i32 s0, 0xffff
	s_waitcnt vmcnt(2)
	v_mov_b32_e32 v10, v2
	v_lshlrev_b64 v[18:19], 10, v[10:11]
	v_mov_b32_e32 v10, v3
	v_lshl_add_u64 v[2:3], v[12:13], 0, v[18:19]
	global_load_dwordx4 v[18:21], v[2:3], off nt
	s_waitcnt vmcnt(2)
	v_lshlrev_b32_e32 v37, 16, v29
	v_lshlrev_b32_e32 v36, 16, v28
	v_and_b32_e32 v39, 0xffff0000, v29
	v_and_b32_e32 v38, 0xffff0000, v28
	v_lshlrev_b64 v[28:29], 10, v[10:11]
	v_mov_b32_e32 v10, v4
	v_lshl_add_u64 v[2:3], v[12:13], 0, v[28:29]
	v_lshlrev_b64 v[28:29], 10, v[10:11]
	v_mov_b32_e32 v10, v5
	s_waitcnt vmcnt(1)
	v_lshlrev_b32_e32 v45, 16, v33
	v_lshlrev_b32_e32 v44, 16, v32
	v_and_b32_e32 v47, 0xffff0000, v33
	v_and_b32_e32 v46, 0xffff0000, v32
	global_load_dwordx4 v[2:5], v[2:3], off nt
	v_lshl_add_u64 v[28:29], v[12:13], 0, v[28:29]
	v_lshlrev_b64 v[32:33], 10, v[10:11]
	v_lshlrev_b32_e32 v41, 16, v31
	v_lshlrev_b32_e32 v40, 16, v30
	v_and_b32_e32 v43, 0xffff0000, v31
	v_and_b32_e32 v42, 0xffff0000, v30
	global_load_dwordx4 v[28:31], v[28:29], off nt
	v_lshl_add_u64 v[32:33], v[12:13], 0, v[32:33]
	v_lshlrev_b32_e32 v49, 16, v35
	v_lshlrev_b32_e32 v48, 16, v34
	v_and_b32_e32 v51, 0xffff0000, v35
	v_and_b32_e32 v50, 0xffff0000, v34
	global_load_dwordx4 v[32:35], v[32:33], off nt
	s_waitcnt vmcnt(3)
	v_cvt_pk_f32_fp8_e32 v[52:53], v18
	v_cvt_pk_f32_fp8_sdwa v[54:55], v18 src0_sel:WORD_1
	v_cvt_pk_f32_fp8_e32 v[56:57], v19
	v_cvt_pk_f32_fp8_sdwa v[18:19], v19 src0_sel:WORD_1
	v_cvt_pk_f32_fp8_e32 v[58:59], v20
	v_cvt_pk_f32_fp8_sdwa v[60:61], v20 src0_sel:WORD_1
	v_cvt_pk_f32_fp8_e32 v[62:63], v21
	v_cvt_pk_f32_fp8_sdwa v[20:21], v21 src0_sel:WORD_1
	v_mov_b32_e32 v100, v52
	v_mov_b32_e32 v101, v54
	v_mov_b32_e32 v54, v53
	v_mov_b32_e32 v52, v56
	v_mov_b32_e32 v53, v18
	v_mov_b32_e32 v18, v57
	s_waitcnt vmcnt(2)
	v_cvt_pk_f32_fp8_e32 v[64:65], v2
	v_cvt_pk_f32_fp8_sdwa v[66:67], v2 src0_sel:WORD_1
	v_cvt_pk_f32_fp8_e32 v[68:69], v3
	v_cvt_pk_f32_fp8_sdwa v[2:3], v3 src0_sel:WORD_1
	v_cvt_pk_f32_fp8_e32 v[70:71], v4
	v_cvt_pk_f32_fp8_sdwa v[72:73], v4 src0_sel:WORD_1
	v_cvt_pk_f32_fp8_e32 v[74:75], v5
	v_cvt_pk_f32_fp8_sdwa v[4:5], v5 src0_sel:WORD_1
	s_waitcnt vmcnt(1)
	v_cvt_pk_f32_fp8_e32 v[76:77], v28
	v_cvt_pk_f32_fp8_sdwa v[78:79], v28 src0_sel:WORD_1
	v_cvt_pk_f32_fp8_e32 v[80:81], v29
	v_cvt_pk_f32_fp8_sdwa v[28:29], v29 src0_sel:WORD_1
	v_cvt_pk_f32_fp8_e32 v[82:83], v30
	v_cvt_pk_f32_fp8_sdwa v[84:85], v30 src0_sel:WORD_1
	v_cvt_pk_f32_fp8_e32 v[86:87], v31
	v_cvt_pk_f32_fp8_sdwa v[30:31], v31 src0_sel:WORD_1
	s_waitcnt vmcnt(0)
	v_cvt_pk_f32_fp8_e32 v[88:89], v32
	v_cvt_pk_f32_fp8_sdwa v[90:91], v32 src0_sel:WORD_1
	v_cvt_pk_f32_fp8_e32 v[92:93], v33
	v_cvt_pk_f32_fp8_sdwa v[32:33], v33 src0_sel:WORD_1
	v_cvt_pk_f32_fp8_e32 v[94:95], v34
	v_cvt_pk_f32_fp8_sdwa v[96:97], v34 src0_sel:WORD_1
	v_cvt_pk_f32_fp8_e32 v[98:99], v35
	v_cvt_pk_f32_fp8_sdwa v[34:35], v35 src0_sel:WORD_1
	v_mov_b32_e32 v56, v58
	v_mov_b32_e32 v57, v60
	v_mov_b32_e32 v60, v59
	v_mov_b32_e32 v58, v62
	v_mov_b32_e32 v59, v20
	v_mov_b32_e32 v20, v63
	v_pk_fma_f32 v[36:37], v[100:101], s[16:17], v[36:37] op_sel_hi:[1,0,1]
	v_pk_fma_f32 v[38:39], v[54:55], s[16:17], v[38:39] op_sel_hi:[1,0,1]
	v_mov_b32_e32 v54, v64
	v_mov_b32_e32 v55, v66
	v_mov_b32_e32 v66, v65
	v_pk_fma_f32 v[40:41], v[52:53], s[16:17], v[40:41] op_sel_hi:[1,0,1]
	v_pk_fma_f32 v[18:19], v[18:19], s[16:17], v[42:43] op_sel_hi:[1,0,1]
	v_mov_b32_e32 v42, v68
	v_mov_b32_e32 v43, v2
	v_mov_b32_e32 v2, v69
	v_pk_fma_f32 v[44:45], v[56:57], s[16:17], v[44:45] op_sel_hi:[1,0,1]
	v_pk_fma_f32 v[46:47], v[60:61], s[16:17], v[46:47] op_sel_hi:[1,0,1]
	v_mov_b32_e32 v52, v70
	v_mov_b32_e32 v53, v72
	v_mov_b32_e32 v72, v71
	v_pk_fma_f32 v[48:49], v[58:59], s[16:17], v[48:49] op_sel_hi:[1,0,1]
	v_pk_fma_f32 v[20:21], v[20:21], s[16:17], v[50:51] op_sel_hi:[1,0,1]
	v_mov_b32_e32 v50, v74
	v_mov_b32_e32 v51, v4
	v_mov_b32_e32 v4, v75
	v_pk_fma_f32 v[36:37], v[54:55], s[16:17], v[36:37] op_sel_hi:[1,0,1]
	v_pk_fma_f32 v[38:39], v[66:67], s[16:17], v[38:39] op_sel_hi:[1,0,1]
	v_mov_b32_e32 v54, v76
	v_mov_b32_e32 v55, v78
	v_mov_b32_e32 v78, v77
	v_pk_fma_f32 v[40:41], v[42:43], s[16:17], v[40:41] op_sel_hi:[1,0,1]
	v_pk_fma_f32 v[2:3], v[2:3], s[16:17], v[18:19] op_sel_hi:[1,0,1]
	v_mov_b32_e32 v18, v80
	v_mov_b32_e32 v19, v28
	v_mov_b32_e32 v28, v81
	v_pk_fma_f32 v[42:43], v[52:53], s[16:17], v[44:45] op_sel_hi:[1,0,1]
	v_pk_fma_f32 v[44:45], v[72:73], s[16:17], v[46:47] op_sel_hi:[1,0,1]
	v_mov_b32_e32 v46, v82
	v_mov_b32_e32 v47, v84
	v_mov_b32_e32 v84, v83
	v_pk_fma_f32 v[48:49], v[50:51], s[16:17], v[48:49] op_sel_hi:[1,0,1]
	v_pk_fma_f32 v[4:5], v[4:5], s[16:17], v[20:21] op_sel_hi:[1,0,1]
	v_mov_b32_e32 v20, v86
	v_mov_b32_e32 v21, v30
	v_mov_b32_e32 v30, v87
	v_pk_fma_f32 v[36:37], v[54:55], s[16:17], v[36:37] op_sel_hi:[1,0,1]
	v_pk_fma_f32 v[38:39], v[78:79], s[16:17], v[38:39] op_sel_hi:[1,0,1]
	v_mov_b32_e32 v50, v88
	v_mov_b32_e32 v51, v90
	v_mov_b32_e32 v90, v89
	v_pk_fma_f32 v[18:19], v[18:19], s[16:17], v[40:41] op_sel_hi:[1,0,1]
	v_pk_fma_f32 v[2:3], v[28:29], s[16:17], v[2:3] op_sel_hi:[1,0,1]
	v_mov_b32_e32 v28, v92
	v_mov_b32_e32 v29, v32
	v_mov_b32_e32 v32, v93
	v_pk_fma_f32 v[40:41], v[46:47], s[16:17], v[42:43] op_sel_hi:[1,0,1]
	v_pk_fma_f32 v[42:43], v[84:85], s[16:17], v[44:45] op_sel_hi:[1,0,1]
	v_mov_b32_e32 v45, v96
	v_mov_b32_e32 v96, v95
	v_pk_fma_f32 v[20:21], v[20:21], s[16:17], v[48:49] op_sel_hi:[1,0,1]
	v_pk_fma_f32 v[4:5], v[30:31], s[16:17], v[4:5] op_sel_hi:[1,0,1]
	v_mov_b32_e32 v30, v98
	v_mov_b32_e32 v31, v34
	v_mov_b32_e32 v34, v99
	v_pk_fma_f32 v[36:37], v[50:51], s[16:17], v[36:37] op_sel_hi:[1,0,1]
	v_pk_fma_f32 v[38:39], v[90:91], s[16:17], v[38:39] op_sel_hi:[1,0,1]
	v_pk_fma_f32 v[28:29], v[28:29], s[16:17], v[18:19] op_sel_hi:[1,0,1]
	v_pk_fma_f32 v[32:33], v[32:33], s[16:17], v[2:3] op_sel_hi:[1,0,1]
	v_pk_fma_f32 v[42:43], v[96:97], s[16:17], v[42:43] op_sel_hi:[1,0,1]
	v_pk_fma_f32 v[30:31], v[30:31], s[16:17], v[20:21] op_sel_hi:[1,0,1]
	v_pk_fma_f32 v[34:35], v[34:35], s[16:17], v[4:5] op_sel_hi:[1,0,1]
	v_pk_mul_f32 v[2:3], v[36:37], v[36:37]
	v_pk_mul_f32 v[18:19], v[38:39], v[38:39]
	v_bfe_u32 v5, v32, 16, 1
	v_bfe_u32 v21, v36, 16, 1
	v_bfe_u32 v56, v37, 16, 1
	v_bfe_u32 v57, v28, 16, 1
	v_bfe_u32 v58, v29, 16, 1
	v_bfe_u32 v4, v33, 16, 1
	v_bfe_u32 v10, v39, 16, 1
	v_bfe_u32 v20, v38, 16, 1
	v_bfe_u32 v62, v42, 16, 1
	v_bfe_u32 v65, v30, 16, 1
	v_add3_u32 v67, v32, v5, s3
	v_add3_u32 v5, v29, v58, s3
	v_add3_u32 v57, v28, v57, s3
	v_add3_u32 v56, v37, v56, s3
	v_add3_u32 v21, v36, v21, s3
	v_add_f32_e32 v2, v2, v18
	v_mov_b32_e32 v44, v94
	v_add3_u32 v20, v38, v20, s3
	v_add3_u32 v10, v39, v10, s3
	v_add3_u32 v4, v33, v4, s3
	v_add3_u32 v18, v42, v62, s3
	v_add3_u32 v62, v30, v65, s3
	v_lshrrev_b32_e32 v21, 16, v21
	v_lshrrev_b32_e32 v56, 16, v56
	v_lshrrev_b32_e32 v57, 16, v57
	v_lshrrev_b32_e32 v5, 16, v5
	v_add_f32_e32 v65, v2, v3
	v_pk_fma_f32 v[40:41], v[44:45], s[16:17], v[40:41] op_sel_hi:[1,0,1]
	v_pk_mul_f32 v[44:45], v[28:29], v[28:29]
	v_and_or_b32 v5, v4, s1, v5
	v_and_or_b32 v4, v67, s1, v57
	v_and_or_b32 v3, v10, s1, v56
	v_and_or_b32 v2, v20, s1, v21
	v_add_f32_e32 v10, v19, v65
	v_pk_mul_f32 v[46:47], v[32:33], v[32:33]
	global_store_dwordx4 v[14:15], v[2:5], off
	v_pk_mul_f32 v[48:49], v[40:41], v[40:41]
	v_pk_mul_f32 v[50:51], v[42:43], v[42:43]
	v_add_f32_e32 v2, v44, v10
	v_add_f32_e32 v2, v46, v2
	v_add_f32_e32 v2, v45, v2
	v_add_f32_e32 v2, v47, v2
	v_add_f32_e32 v2, v48, v2
	v_add_f32_e32 v2, v50, v2
	v_add_f32_e32 v2, v49, v2
	v_pk_mul_f32 v[52:53], v[30:31], v[30:31]
	v_add_f32_e32 v2, v51, v2
	v_pk_mul_f32 v[54:55], v[34:35], v[34:35]
	v_add_f32_e32 v2, v52, v2
	v_add_f32_e32 v2, v54, v2
	v_add_f32_e32 v2, v53, v2
	v_add_f32_e32 v2, v55, v2
	ds_bpermute_b32 v3, v1, v2
	v_bfe_u32 v59, v35, 16, 1
	v_bfe_u32 v61, v43, 16, 1
	v_bfe_u32 v66, v31, 16, 1
	v_add3_u32 v58, v43, v61, s3
	s_waitcnt lgkmcnt(0)
	v_add_f32_e32 v2, v2, v3
	ds_bpermute_b32 v3, v22, v2
	v_add3_u32 v59, v35, v59, s3
	v_add3_u32 v61, v31, v66, s3
	v_bfe_u32 v63, v40, 16, 1
	v_bfe_u32 v64, v41, 16, 1
	s_waitcnt lgkmcnt(0)
	v_add_f32_e32 v2, v2, v3
	ds_bpermute_b32 v3, v23, v2
	v_bfe_u32 v60, v34, 16, 1
	v_add3_u32 v64, v41, v64, s3
	v_add3_u32 v63, v40, v63, s3
	v_add3_u32 v60, v34, v60, s3
	s_waitcnt lgkmcnt(0)
	v_add_f32_e32 v2, v2, v3
	ds_bpermute_b32 v3, v24, v2
	v_lshrrev_b32_e32 v63, 16, v63
	v_lshrrev_b32_e32 v64, 16, v64
	v_lshrrev_b32_e32 v62, 16, v62
	v_lshrrev_b32_e32 v61, 16, v61
	s_waitcnt lgkmcnt(0)
	v_add_f32_e32 v2, v2, v3
	ds_bpermute_b32 v3, v25, v2
	v_and_or_b32 v21, v59, s1, v61
	v_and_or_b32 v20, v60, s1, v62
	v_and_or_b32 v19, v58, s1, v64
	v_and_or_b32 v18, v18, s1, v63
	s_waitcnt lgkmcnt(0)
	v_add_f32_e32 v2, v2, v3
	ds_bpermute_b32 v3, v26, v2
	global_store_dwordx4 v[14:15], v[18:21], off offset:16
	v_lshl_add_u64 v[14:15], v[14:15], 0, s[6:7]
	s_waitcnt lgkmcnt(0)
	v_add_f32_e32 v2, v2, v3
	v_fmamk_f32 v2, v2, 0x3a800000, v27
	v_rsq_f32_e32 v2, v2
	s_nop 0
	v_mul_f32_e32 v3, v37, v2
	v_mul_f32_e32 v4, v39, v2
	v_mul_f32_e32 v5, v36, v2
	v_mul_f32_e32 v10, v38, v2
	v_mul_f32_e32 v29, v29, v2
	v_mul_f32_e32 v33, v33, v2
	v_mul_f32_e32 v28, v28, v2
	v_mul_f32_e32 v32, v32, v2
	v_mul_f32_e32 v36, v41, v2
	v_mul_f32_e32 v37, v43, v2
	v_mul_f32_e32 v38, v40, v2
	v_mul_f32_e32 v39, v42, v2
	v_mul_f32_e32 v31, v31, v2
	v_mul_f32_e32 v35, v35, v2
	v_mul_f32_e32 v30, v30, v2
	v_mul_f32_e32 v2, v34, v2
	v_cvt_pk_fp8_f32 v6, v5, v10
	v_cvt_pk_fp8_f32 v7, v28, v32
	v_cvt_pk_fp8_f32 v8, v38, v39
	v_cvt_pk_fp8_f32 v9, v30, v2
	v_cvt_pk_fp8_f32 v6, v3, v4 op_sel:[0,0,1]
	v_cvt_pk_fp8_f32 v7, v29, v33 op_sel:[0,0,1]
	v_cvt_pk_fp8_f32 v8, v36, v37 op_sel:[0,0,1]
	v_cvt_pk_fp8_f32 v9, v31, v35 op_sel:[0,0,1]
	global_store_dwordx4 v[16:17], v[6:9], off
	v_lshl_add_u64 v[16:17], v[16:17], 0, s[12:13]
	s_cbranch_scc0 .LBB0_1685

.LBB0_3487:
	global_load_dwordx4 v[2:5], v11, s[10:11] nt
	v_add_co_u32_e32 v20, vcc, -0.5, v14
	v_lshl_add_u64 v[18:19], v[14:15], 0, s[16:17]
	s_nop 0
	v_addc_co_u32_e32 v21, vcc, -1, v15, vcc
	global_load_dwordx4 v[28:31], v[20:21], off nt
	global_load_dwordx4 v[32:35], v[18:19], off offset:16 nt
	v_mov_b32_e32 v6, v11
	v_mov_b32_e32 v7, v11
	v_mov_b32_e32 v8, v11
	v_mov_b32_e32 v9, v11
	s_add_i32 s0, s0, s54
	s_add_u32 s10, s10, s12
	s_addc_u32 s11, s11, s13
	s_cmp_gt_i32 s0, 0xffff
	s_waitcnt vmcnt(2)
	v_mov_b32_e32 v10, v2
	v_lshlrev_b64 v[18:19], 10, v[10:11]
	v_mov_b32_e32 v10, v3
	v_lshl_add_u64 v[2:3], v[12:13], 0, v[18:19]
	global_load_dwordx4 v[18:21], v[2:3], off nt
	s_waitcnt vmcnt(2)
	v_lshlrev_b32_e32 v37, 16, v29
	v_lshlrev_b32_e32 v36, 16, v28
	v_and_b32_e32 v39, 0xffff0000, v29
	v_and_b32_e32 v38, 0xffff0000, v28
	v_lshlrev_b64 v[28:29], 10, v[10:11]
	v_mov_b32_e32 v10, v4
	v_lshl_add_u64 v[2:3], v[12:13], 0, v[28:29]
	v_lshlrev_b64 v[28:29], 10, v[10:11]
	v_mov_b32_e32 v10, v5
	s_waitcnt vmcnt(1)
	v_lshlrev_b32_e32 v45, 16, v33
	v_lshlrev_b32_e32 v44, 16, v32
	v_and_b32_e32 v47, 0xffff0000, v33
	v_and_b32_e32 v46, 0xffff0000, v32
	global_load_dwordx4 v[2:5], v[2:3], off nt
	v_lshl_add_u64 v[28:29], v[12:13], 0, v[28:29]
	v_lshlrev_b64 v[32:33], 10, v[10:11]
	v_lshlrev_b32_e32 v41, 16, v31
	v_lshlrev_b32_e32 v40, 16, v30
	v_and_b32_e32 v43, 0xffff0000, v31
	v_and_b32_e32 v42, 0xffff0000, v30
	global_load_dwordx4 v[28:31], v[28:29], off nt
	v_lshl_add_u64 v[32:33], v[12:13], 0, v[32:33]
	v_lshlrev_b32_e32 v49, 16, v35
	v_lshlrev_b32_e32 v48, 16, v34
	v_and_b32_e32 v51, 0xffff0000, v35
	v_and_b32_e32 v50, 0xffff0000, v34
	global_load_dwordx4 v[32:35], v[32:33], off nt
	s_waitcnt vmcnt(3)
	v_cvt_pk_f32_fp8_e32 v[52:53], v18
	v_cvt_pk_f32_fp8_sdwa v[54:55], v18 src0_sel:WORD_1
	v_cvt_pk_f32_fp8_e32 v[56:57], v19
	v_cvt_pk_f32_fp8_sdwa v[18:19], v19 src0_sel:WORD_1
	v_cvt_pk_f32_fp8_e32 v[58:59], v20
	v_cvt_pk_f32_fp8_sdwa v[60:61], v20 src0_sel:WORD_1
	v_cvt_pk_f32_fp8_e32 v[62:63], v21
	v_cvt_pk_f32_fp8_sdwa v[20:21], v21 src0_sel:WORD_1
	v_mov_b32_e32 v100, v52
	v_mov_b32_e32 v101, v54
	v_mov_b32_e32 v54, v53
	v_mov_b32_e32 v52, v56
	v_mov_b32_e32 v53, v18
	v_mov_b32_e32 v18, v57
	s_waitcnt vmcnt(2)
	v_cvt_pk_f32_fp8_e32 v[64:65], v2
	v_cvt_pk_f32_fp8_sdwa v[66:67], v2 src0_sel:WORD_1
	v_cvt_pk_f32_fp8_e32 v[68:69], v3
	v_cvt_pk_f32_fp8_sdwa v[2:3], v3 src0_sel:WORD_1
	v_cvt_pk_f32_fp8_e32 v[70:71], v4
	v_cvt_pk_f32_fp8_sdwa v[72:73], v4 src0_sel:WORD_1
	v_cvt_pk_f32_fp8_e32 v[74:75], v5
	v_cvt_pk_f32_fp8_sdwa v[4:5], v5 src0_sel:WORD_1
	s_waitcnt vmcnt(1)
	v_cvt_pk_f32_fp8_e32 v[76:77], v28
	v_cvt_pk_f32_fp8_sdwa v[78:79], v28 src0_sel:WORD_1
	v_cvt_pk_f32_fp8_e32 v[80:81], v29
	v_cvt_pk_f32_fp8_sdwa v[28:29], v29 src0_sel:WORD_1
	v_cvt_pk_f32_fp8_e32 v[82:83], v30
	v_cvt_pk_f32_fp8_sdwa v[84:85], v30 src0_sel:WORD_1
	v_cvt_pk_f32_fp8_e32 v[86:87], v31
	v_cvt_pk_f32_fp8_sdwa v[30:31], v31 src0_sel:WORD_1
	s_waitcnt vmcnt(0)
	v_cvt_pk_f32_fp8_e32 v[88:89], v32
	v_cvt_pk_f32_fp8_sdwa v[90:91], v32 src0_sel:WORD_1
	v_cvt_pk_f32_fp8_e32 v[92:93], v33
	v_cvt_pk_f32_fp8_sdwa v[32:33], v33 src0_sel:WORD_1
	v_cvt_pk_f32_fp8_e32 v[94:95], v34
	v_cvt_pk_f32_fp8_sdwa v[96:97], v34 src0_sel:WORD_1
	v_cvt_pk_f32_fp8_e32 v[98:99], v35
	v_cvt_pk_f32_fp8_sdwa v[34:35], v35 src0_sel:WORD_1
	v_mov_b32_e32 v56, v58
	v_mov_b32_e32 v57, v60
	v_mov_b32_e32 v60, v59
	v_mov_b32_e32 v58, v62
	v_mov_b32_e32 v59, v20
	v_mov_b32_e32 v20, v63
	v_pk_fma_f32 v[36:37], v[100:101], s[18:19], v[36:37] op_sel_hi:[1,0,1]
	v_pk_fma_f32 v[38:39], v[54:55], s[18:19], v[38:39] op_sel_hi:[1,0,1]
	v_mov_b32_e32 v54, v64
	v_mov_b32_e32 v55, v66
	v_mov_b32_e32 v66, v65
	v_pk_fma_f32 v[40:41], v[52:53], s[18:19], v[40:41] op_sel_hi:[1,0,1]
	v_pk_fma_f32 v[18:19], v[18:19], s[18:19], v[42:43] op_sel_hi:[1,0,1]
	v_mov_b32_e32 v42, v68
	v_mov_b32_e32 v43, v2
	v_mov_b32_e32 v2, v69
	v_pk_fma_f32 v[44:45], v[56:57], s[18:19], v[44:45] op_sel_hi:[1,0,1]
	v_pk_fma_f32 v[46:47], v[60:61], s[18:19], v[46:47] op_sel_hi:[1,0,1]
	v_mov_b32_e32 v52, v70
	v_mov_b32_e32 v53, v72
	v_mov_b32_e32 v72, v71
	v_pk_fma_f32 v[48:49], v[58:59], s[18:19], v[48:49] op_sel_hi:[1,0,1]
	v_pk_fma_f32 v[20:21], v[20:21], s[18:19], v[50:51] op_sel_hi:[1,0,1]
	v_mov_b32_e32 v50, v74
	v_mov_b32_e32 v51, v4
	v_mov_b32_e32 v4, v75
	v_pk_fma_f32 v[36:37], v[54:55], s[18:19], v[36:37] op_sel_hi:[1,0,1]
	v_pk_fma_f32 v[38:39], v[66:67], s[18:19], v[38:39] op_sel_hi:[1,0,1]
	v_mov_b32_e32 v54, v76
	v_mov_b32_e32 v55, v78
	v_mov_b32_e32 v78, v77
	v_pk_fma_f32 v[40:41], v[42:43], s[18:19], v[40:41] op_sel_hi:[1,0,1]
	v_pk_fma_f32 v[2:3], v[2:3], s[18:19], v[18:19] op_sel_hi:[1,0,1]
	v_mov_b32_e32 v18, v80
	v_mov_b32_e32 v19, v28
	v_mov_b32_e32 v28, v81
	v_pk_fma_f32 v[42:43], v[52:53], s[18:19], v[44:45] op_sel_hi:[1,0,1]
	v_pk_fma_f32 v[44:45], v[72:73], s[18:19], v[46:47] op_sel_hi:[1,0,1]
	v_mov_b32_e32 v46, v82
	v_mov_b32_e32 v47, v84
	v_mov_b32_e32 v84, v83
	v_pk_fma_f32 v[48:49], v[50:51], s[18:19], v[48:49] op_sel_hi:[1,0,1]
	v_pk_fma_f32 v[4:5], v[4:5], s[18:19], v[20:21] op_sel_hi:[1,0,1]
	v_mov_b32_e32 v20, v86
	v_mov_b32_e32 v21, v30
	v_mov_b32_e32 v30, v87
	v_pk_fma_f32 v[36:37], v[54:55], s[18:19], v[36:37] op_sel_hi:[1,0,1]
	v_pk_fma_f32 v[38:39], v[78:79], s[18:19], v[38:39] op_sel_hi:[1,0,1]
	v_mov_b32_e32 v50, v88
	v_mov_b32_e32 v51, v90
	v_mov_b32_e32 v90, v89
	v_pk_fma_f32 v[18:19], v[18:19], s[18:19], v[40:41] op_sel_hi:[1,0,1]
	v_pk_fma_f32 v[2:3], v[28:29], s[18:19], v[2:3] op_sel_hi:[1,0,1]
	v_mov_b32_e32 v28, v92
	v_mov_b32_e32 v29, v32
	v_mov_b32_e32 v32, v93
	v_pk_fma_f32 v[40:41], v[46:47], s[18:19], v[42:43] op_sel_hi:[1,0,1]
	v_pk_fma_f32 v[42:43], v[84:85], s[18:19], v[44:45] op_sel_hi:[1,0,1]
	v_mov_b32_e32 v45, v96
	v_mov_b32_e32 v96, v95
	v_pk_fma_f32 v[20:21], v[20:21], s[18:19], v[48:49] op_sel_hi:[1,0,1]
	v_pk_fma_f32 v[4:5], v[30:31], s[18:19], v[4:5] op_sel_hi:[1,0,1]
	v_mov_b32_e32 v30, v98
	v_mov_b32_e32 v31, v34
	v_mov_b32_e32 v34, v99
	v_pk_fma_f32 v[36:37], v[50:51], s[18:19], v[36:37] op_sel_hi:[1,0,1]
	v_pk_fma_f32 v[38:39], v[90:91], s[18:19], v[38:39] op_sel_hi:[1,0,1]
	v_pk_fma_f32 v[28:29], v[28:29], s[18:19], v[18:19] op_sel_hi:[1,0,1]
	v_pk_fma_f32 v[32:33], v[32:33], s[18:19], v[2:3] op_sel_hi:[1,0,1]
	v_pk_fma_f32 v[42:43], v[96:97], s[18:19], v[42:43] op_sel_hi:[1,0,1]
	v_pk_fma_f32 v[30:31], v[30:31], s[18:19], v[20:21] op_sel_hi:[1,0,1]
	v_pk_fma_f32 v[34:35], v[34:35], s[18:19], v[4:5] op_sel_hi:[1,0,1]
	v_pk_mul_f32 v[2:3], v[36:37], v[36:37]
	v_pk_mul_f32 v[18:19], v[38:39], v[38:39]
	v_bfe_u32 v5, v32, 16, 1
	v_bfe_u32 v21, v36, 16, 1
	v_bfe_u32 v56, v37, 16, 1
	v_bfe_u32 v57, v28, 16, 1
	v_bfe_u32 v58, v29, 16, 1
	v_bfe_u32 v4, v33, 16, 1
	v_bfe_u32 v10, v39, 16, 1
	v_bfe_u32 v20, v38, 16, 1
	v_bfe_u32 v62, v42, 16, 1
	v_bfe_u32 v65, v30, 16, 1
	v_add3_u32 v67, v32, v5, s3
	v_add3_u32 v5, v29, v58, s3
	v_add3_u32 v57, v28, v57, s3
	v_add3_u32 v56, v37, v56, s3
	v_add3_u32 v21, v36, v21, s3
	v_add_f32_e32 v2, v2, v18
	v_mov_b32_e32 v44, v94
	v_add3_u32 v20, v38, v20, s3
	v_add3_u32 v10, v39, v10, s3
	v_add3_u32 v4, v33, v4, s3
	v_add3_u32 v18, v42, v62, s3
	v_add3_u32 v62, v30, v65, s3
	v_lshrrev_b32_e32 v21, 16, v21
	v_lshrrev_b32_e32 v56, 16, v56
	v_lshrrev_b32_e32 v57, 16, v57
	v_lshrrev_b32_e32 v5, 16, v5
	v_add_f32_e32 v65, v2, v3
	v_pk_fma_f32 v[40:41], v[44:45], s[18:19], v[40:41] op_sel_hi:[1,0,1]
	v_pk_mul_f32 v[44:45], v[28:29], v[28:29]
	v_and_or_b32 v5, v4, s1, v5
	v_and_or_b32 v4, v67, s1, v57
	v_and_or_b32 v3, v10, s1, v56
	v_and_or_b32 v2, v20, s1, v21
	v_add_f32_e32 v10, v19, v65
	v_pk_mul_f32 v[46:47], v[32:33], v[32:33]
	global_store_dwordx4 v[14:15], v[2:5], off
	v_pk_mul_f32 v[48:49], v[40:41], v[40:41]
	v_pk_mul_f32 v[50:51], v[42:43], v[42:43]
	v_add_f32_e32 v2, v44, v10
	v_add_f32_e32 v2, v46, v2
	v_add_f32_e32 v2, v45, v2
	v_add_f32_e32 v2, v47, v2
	v_add_f32_e32 v2, v48, v2
	v_add_f32_e32 v2, v50, v2
	v_add_f32_e32 v2, v49, v2
	v_pk_mul_f32 v[52:53], v[30:31], v[30:31]
	v_add_f32_e32 v2, v51, v2
	v_pk_mul_f32 v[54:55], v[34:35], v[34:35]
	v_add_f32_e32 v2, v52, v2
	v_add_f32_e32 v2, v54, v2
	v_add_f32_e32 v2, v53, v2
	v_add_f32_e32 v2, v55, v2
	ds_bpermute_b32 v3, v1, v2
	v_bfe_u32 v59, v35, 16, 1
	v_bfe_u32 v61, v43, 16, 1
	v_bfe_u32 v66, v31, 16, 1
	v_add3_u32 v58, v43, v61, s3
	s_waitcnt lgkmcnt(0)
	v_add_f32_e32 v2, v2, v3
	ds_bpermute_b32 v3, v22, v2
	v_add3_u32 v59, v35, v59, s3
	v_add3_u32 v61, v31, v66, s3
	v_bfe_u32 v63, v40, 16, 1
	v_bfe_u32 v64, v41, 16, 1
	s_waitcnt lgkmcnt(0)
	v_add_f32_e32 v2, v2, v3
	ds_bpermute_b32 v3, v23, v2
	v_bfe_u32 v60, v34, 16, 1
	v_add3_u32 v64, v41, v64, s3
	v_add3_u32 v63, v40, v63, s3
	v_add3_u32 v60, v34, v60, s3
	s_waitcnt lgkmcnt(0)
	v_add_f32_e32 v2, v2, v3
	ds_bpermute_b32 v3, v24, v2
	v_lshrrev_b32_e32 v63, 16, v63
	v_lshrrev_b32_e32 v64, 16, v64
	v_lshrrev_b32_e32 v62, 16, v62
	v_lshrrev_b32_e32 v61, 16, v61
	s_waitcnt lgkmcnt(0)
	v_add_f32_e32 v2, v2, v3
	ds_bpermute_b32 v3, v25, v2
	v_and_or_b32 v21, v59, s1, v61
	v_and_or_b32 v20, v60, s1, v62
	v_and_or_b32 v19, v58, s1, v64
	v_and_or_b32 v18, v18, s1, v63
	s_waitcnt lgkmcnt(0)
	v_add_f32_e32 v2, v2, v3
	ds_bpermute_b32 v3, v26, v2
	global_store_dwordx4 v[14:15], v[18:21], off offset:16
	v_lshl_add_u64 v[14:15], v[14:15], 0, s[8:9]
	s_waitcnt lgkmcnt(0)
	v_add_f32_e32 v2, v2, v3
	v_fmamk_f32 v2, v2, 0x3a800000, v27
	v_rsq_f32_e32 v2, v2
	s_nop 0
	v_mul_f32_e32 v3, v37, v2
	v_mul_f32_e32 v4, v39, v2
	v_mul_f32_e32 v5, v36, v2
	v_mul_f32_e32 v10, v38, v2
	v_mul_f32_e32 v29, v29, v2
	v_mul_f32_e32 v33, v33, v2
	v_mul_f32_e32 v28, v28, v2
	v_mul_f32_e32 v32, v32, v2
	v_mul_f32_e32 v36, v41, v2
	v_mul_f32_e32 v37, v43, v2
	v_mul_f32_e32 v38, v40, v2
	v_mul_f32_e32 v39, v42, v2
	v_mul_f32_e32 v31, v31, v2
	v_mul_f32_e32 v35, v35, v2
	v_mul_f32_e32 v30, v30, v2
	v_mul_f32_e32 v2, v34, v2
	v_cvt_pk_fp8_f32 v6, v5, v10
	v_cvt_pk_fp8_f32 v7, v28, v32
	v_cvt_pk_fp8_f32 v8, v38, v39
	v_cvt_pk_fp8_f32 v9, v30, v2
	v_cvt_pk_fp8_f32 v6, v3, v4 op_sel:[0,0,1]
	v_cvt_pk_fp8_f32 v7, v29, v33 op_sel:[0,0,1]
	v_cvt_pk_fp8_f32 v8, v36, v37 op_sel:[0,0,1]
	v_cvt_pk_fp8_f32 v9, v31, v35 op_sel:[0,0,1]
	global_store_dwordx4 v[16:17], v[6:9], off
	v_lshl_add_u64 v[16:17], v[16:17], 0, s[14:15]
	s_cbranch_scc0 .LBB0_3487

.LBB0_3638:
	s_or_b64 exec, exec, s[6:7]
	s_lshr_b32 s1, s97, 3
	s_mul_i32 s1, s1, s64
	v_readlane_b32 s3, v254, 12
	s_and_b32 s0, s97, 7
	s_add_i32 s1, s1, s3
	s_cmp_eq_u32 s0, 0
	s_cselect_b32 s0, s1, s2
	s_waitcnt lgkmcnt(0)
	s_barrier
	s_lshl_b32 s1, s0, 3
	s_nop 0
	v_readfirstlane_b32 s0, v0
	s_lshl_b32 s13, s97, 3
	s_ashr_i32 s2, s0, 6
	s_add_i32 s12, s2, s1
	s_cmp_lt_i32 s12, 0x10000
	s_cbranch_scc0 .LBB0_3641
	s_load_dwordx4 s[4:7], s[90:91], 0xc0
	s_load_dwordx2 s[8:9], s[90:91], 0x28
	v_and_b32_e32 v1, 63, v0
	v_lshlrev_b32_e32 v2, 4, v1
	v_lshlrev_b32_e32 v3, 3, v1
	v_and_b32_e32 v4, 15, v1
	v_lshlrev_b32_e32 v4, 18, v4
	v_mov_b32_e32 v5, 0x358637bd
	s_lshl_b32 s20, s13, 2
	s_lshl_b32 s21, s13, 11
	s_lshl_b32 s22, s13, 12
	s_mul_i32 s23, s13, 7
	s_waitcnt lgkmcnt(0)
	global_load_dwordx4 v[8:11], v2, s[8:9] offset:0
	global_load_dwordx4 v[12:15], v2, s[8:9] offset:1024
	global_load_dwordx4 v[16:19], v2, s[8:9] offset:2048
	global_load_dwordx4 v[20:23], v2, s[8:9] offset:3072
	s_ashr_i32 s15, s12, 31
	s_mov_b32 s14, s12
	s_lshl_b64 s[16:17], s[14:15], 2
	s_add_u32 s16, s16, 0x72000000
	s_addc_u32 s17, s17, 0
	s_add_u32 s16, s16, s6
	s_addc_u32 s17, s17, s7
	s_lshl_b64 s[18:19], s[14:15], 11
	s_add_u32 s18, s18, 0x26c00000
	s_addc_u32 s19, s19, 0
	s_add_u32 s18, s18, s6
	s_addc_u32 s19, s19, s7
	s_lshl_b64 s[24:25], s[14:15], 12
	s_add_u32 s24, s24, s4
	s_addc_u32 s25, s25, s5
	s_add_i32 s14, s12, s23
	s_cmp_lt_i32 s14, 0x10000
	s_cbranch_scc0 .Lfin_tail
	s_mov_b64 s[26:27], s[16:17]
	s_mov_b64 s[28:29], s[18:19]
	global_load_dword v40, v4, s[26:27]
	global_load_dwordx2 v[32:33], v3, s[28:29] offset:0 nt
	global_load_dwordx2 v[34:35], v3, s[28:29] offset:512 nt
	global_load_dwordx2 v[36:37], v3, s[28:29] offset:1024 nt
	global_load_dwordx2 v[38:39], v3, s[28:29] offset:1536 nt
	s_add_u32 s16, s16, s20
	s_addc_u32 s17, s17, 0
	s_add_u32 s18, s18, s21
	s_addc_u32 s19, s19, 0
	s_add_i32 s12, s12, s13
	s_mov_b64 s[30:31], s[16:17]
	s_mov_b64 s[32:33], s[18:19]
	global_load_dword v50, v4, s[30:31]
	global_load_dwordx2 v[42:43], v3, s[32:33] offset:0 nt
	global_load_dwordx2 v[44:45], v3, s[32:33] offset:512 nt
	global_load_dwordx2 v[46:47], v3, s[32:33] offset:1024 nt
	global_load_dwordx2 v[48:49], v3, s[32:33] offset:1536 nt
	s_add_u32 s16, s16, s20
	s_addc_u32 s17, s17, 0
	s_add_u32 s18, s18, s21
	s_addc_u32 s19, s19, 0
	s_add_i32 s12, s12, s13
	s_mov_b64 s[26:27], s[16:17]
	s_mov_b64 s[28:29], s[18:19]
	global_load_dword v60, v4, s[26:27]
	global_load_dwordx2 v[52:53], v3, s[28:29] offset:0 nt
	global_load_dwordx2 v[54:55], v3, s[28:29] offset:512 nt
	global_load_dwordx2 v[56:57], v3, s[28:29] offset:1024 nt
	global_load_dwordx2 v[58:59], v3, s[28:29] offset:1536 nt
	s_add_u32 s16, s16, s20
	s_addc_u32 s17, s17, 0
	s_add_u32 s18, s18, s21
	s_addc_u32 s19, s19, 0
	s_add_i32 s12, s12, s13
	s_mov_b64 s[30:31], s[16:17]
	s_mov_b64 s[32:33], s[18:19]
	global_load_dword v70, v4, s[30:31]
	global_load_dwordx2 v[62:63], v3, s[32:33] offset:0 nt
	global_load_dwordx2 v[64:65], v3, s[32:33] offset:512 nt
	global_load_dwordx2 v[66:67], v3, s[32:33] offset:1024 nt
	global_load_dwordx2 v[68:69], v3, s[32:33] offset:1536 nt
	s_add_u32 s16, s16, s20
	s_addc_u32 s17, s17, 0
	s_add_u32 s18, s18, s21
	s_addc_u32 s19, s19, 0
	s_add_i32 s12, s12, s13
	s_mov_b64 s[26:27], s[16:17]
	s_mov_b64 s[28:29], s[18:19]
	global_load_dword v80, v4, s[26:27]
	global_load_dwordx2 v[72:73], v3, s[28:29] offset:0 nt
	global_load_dwordx2 v[74:75], v3, s[28:29] offset:512 nt
	global_load_dwordx2 v[76:77], v3, s[28:29] offset:1024 nt
	global_load_dwordx2 v[78:79], v3, s[28:29] offset:1536 nt
	s_add_u32 s16, s16, s20
	s_addc_u32 s17, s17, 0
	s_add_u32 s18, s18, s21
	s_addc_u32 s19, s19, 0
	s_add_i32 s12, s12, s13
	s_mov_b64 s[30:31], s[16:17]
	s_mov_b64 s[32:33], s[18:19]
	global_load_dword v90, v4, s[30:31]
	global_load_dwordx2 v[82:83], v3, s[32:33] offset:0 nt
	global_load_dwordx2 v[84:85], v3, s[32:33] offset:512 nt
	global_load_dwordx2 v[86:87], v3, s[32:33] offset:1024 nt
	global_load_dwordx2 v[88:89], v3, s[32:33] offset:1536 nt
	s_add_u32 s16, s16, s20
	s_addc_u32 s17, s17, 0
	s_add_u32 s18, s18, s21
	s_addc_u32 s19, s19, 0
	s_add_i32 s12, s12, s13
	s_mov_b64 s[26:27], s[16:17]
	s_mov_b64 s[28:29], s[18:19]
	global_load_dword v100, v4, s[26:27]
	global_load_dwordx2 v[92:93], v3, s[28:29] offset:0 nt
	global_load_dwordx2 v[94:95], v3, s[28:29] offset:512 nt
	global_load_dwordx2 v[96:97], v3, s[28:29] offset:1024 nt
	global_load_dwordx2 v[98:99], v3, s[28:29] offset:1536 nt
	s_add_u32 s16, s16, s20
	s_addc_u32 s17, s17, 0
	s_add_u32 s18, s18, s21
	s_addc_u32 s19, s19, 0
	s_add_i32 s12, s12, s13
	s_mov_b64 s[30:31], s[16:17]
	s_mov_b64 s[32:33], s[18:19]
	global_load_dword v110, v4, s[30:31]
	global_load_dwordx2 v[102:103], v3, s[32:33] offset:0 nt
	global_load_dwordx2 v[104:105], v3, s[32:33] offset:512 nt
	global_load_dwordx2 v[106:107], v3, s[32:33] offset:1024 nt
	global_load_dwordx2 v[108:109], v3, s[32:33] offset:1536 nt
	s_add_u32 s16, s16, s20
	s_addc_u32 s17, s17, 0
	s_add_u32 s18, s18, s21
	s_addc_u32 s19, s19, 0
	s_add_i32 s12, s12, s13
	s_waitcnt vmcnt(35)
	v_add_f32_dpp v112, v40, v40 quad_perm:[1,0,3,2] row_mask:0xf bank_mask:0xf
	s_mov_b64 s[34:35], s[24:25]
	s_add_u32 s24, s24, s22
	v_add_f32_dpp v112, v112, v112 quad_perm:[2,3,0,1] row_mask:0xf bank_mask:0xf
	s_addc_u32 s25, s25, 0
	s_nop 0
	v_add_f32_dpp v112, v112, v112 row_half_mirror row_mask:0xf bank_mask:0xf
	s_nop 1
	v_add_f32_dpp v112, v112, v112 row_mirror row_mask:0xf bank_mask:0xf
	v_fmamk_f32 v112, v112, 0x3a800000, v5
	v_rsq_f32_e32 v114, v112
	v_lshlrev_b32_e32 v116, 16, v32
	v_and_b32_e32 v117, 0xffff0000, v32
	v_lshlrev_b32_e32 v118, 16, v33
	v_and_b32_e32 v119, 0xffff0000, v33
	v_lshlrev_b32_e32 v120, 16, v34
	v_and_b32_e32 v121, 0xffff0000, v34
	v_lshlrev_b32_e32 v122, 16, v35
	v_and_b32_e32 v123, 0xffff0000, v35
	v_lshlrev_b32_e32 v124, 16, v36
	v_and_b32_e32 v125, 0xffff0000, v36
	v_lshlrev_b32_e32 v126, 16, v37
	v_and_b32_e32 v127, 0xffff0000, v37
	v_lshlrev_b32_e32 v128, 16, v38
	v_and_b32_e32 v129, 0xffff0000, v38
	v_lshlrev_b32_e32 v130, 16, v39
	v_and_b32_e32 v131, 0xffff0000, v39
	v_pk_mul_f32 v[116:117], v[114:115], v[116:117] op_sel_hi:[0,1]
	v_pk_mul_f32 v[118:119], v[114:115], v[118:119] op_sel_hi:[0,1]
	v_pk_mul_f32 v[120:121], v[114:115], v[120:121] op_sel_hi:[0,1]
	v_pk_mul_f32 v[122:123], v[114:115], v[122:123] op_sel_hi:[0,1]
	v_pk_mul_f32 v[124:125], v[114:115], v[124:125] op_sel_hi:[0,1]
	v_pk_mul_f32 v[126:127], v[114:115], v[126:127] op_sel_hi:[0,1]
	v_pk_mul_f32 v[128:129], v[114:115], v[128:129] op_sel_hi:[0,1]
	v_pk_mul_f32 v[130:131], v[114:115], v[130:131] op_sel_hi:[0,1]
	v_pk_mul_f32 v[132:133], v[8:9], v[116:117]
	v_pk_mul_f32 v[134:135], v[10:11], v[118:119]
	v_pk_mul_f32 v[136:137], v[12:13], v[120:121]
	v_pk_mul_f32 v[138:139], v[14:15], v[122:123]
	v_pk_mul_f32 v[140:141], v[16:17], v[124:125]
	v_pk_mul_f32 v[142:143], v[18:19], v[126:127]
	v_pk_mul_f32 v[144:145], v[20:21], v[128:129]
	v_pk_mul_f32 v[146:147], v[22:23], v[130:131]
	global_store_dwordx4 v2, v[132:135], s[34:35] offset:0 sc1
	global_store_dwordx4 v2, v[136:139], s[34:35] offset:1024 sc1
	global_store_dwordx4 v2, v[140:143], s[34:35] offset:2048 sc1
	global_store_dwordx4 v2, v[144:147], s[34:35] offset:3072 sc1
	s_waitcnt vmcnt(34)
	v_add_f32_dpp v112, v50, v50 quad_perm:[1,0,3,2] row_mask:0xf bank_mask:0xf
	s_mov_b64 s[36:37], s[24:25]
	s_add_u32 s24, s24, s22
	v_add_f32_dpp v112, v112, v112 quad_perm:[2,3,0,1] row_mask:0xf bank_mask:0xf
	s_addc_u32 s25, s25, 0
	s_nop 0
	v_add_f32_dpp v112, v112, v112 row_half_mirror row_mask:0xf bank_mask:0xf
	s_nop 1
	v_add_f32_dpp v112, v112, v112 row_mirror row_mask:0xf bank_mask:0xf
	v_fmamk_f32 v112, v112, 0x3a800000, v5
	v_rsq_f32_e32 v114, v112
	v_lshlrev_b32_e32 v116, 16, v42
	v_and_b32_e32 v117, 0xffff0000, v42
	v_lshlrev_b32_e32 v118, 16, v43
	v_and_b32_e32 v119, 0xffff0000, v43
	v_lshlrev_b32_e32 v120, 16, v44
	v_and_b32_e32 v121, 0xffff0000, v44
	v_lshlrev_b32_e32 v122, 16, v45
	v_and_b32_e32 v123, 0xffff0000, v45
	v_lshlrev_b32_e32 v124, 16, v46
	v_and_b32_e32 v125, 0xffff0000, v46
	v_lshlrev_b32_e32 v126, 16, v47
	v_and_b32_e32 v127, 0xffff0000, v47
	v_lshlrev_b32_e32 v128, 16, v48
	v_and_b32_e32 v129, 0xffff0000, v48
	v_lshlrev_b32_e32 v130, 16, v49
	v_and_b32_e32 v131, 0xffff0000, v49
	v_pk_mul_f32 v[116:117], v[114:115], v[116:117] op_sel_hi:[0,1]
	v_pk_mul_f32 v[118:119], v[114:115], v[118:119] op_sel_hi:[0,1]
	v_pk_mul_f32 v[120:121], v[114:115], v[120:121] op_sel_hi:[0,1]
	v_pk_mul_f32 v[122:123], v[114:115], v[122:123] op_sel_hi:[0,1]
	v_pk_mul_f32 v[124:125], v[114:115], v[124:125] op_sel_hi:[0,1]
	v_pk_mul_f32 v[126:127], v[114:115], v[126:127] op_sel_hi:[0,1]
	v_pk_mul_f32 v[128:129], v[114:115], v[128:129] op_sel_hi:[0,1]
	v_pk_mul_f32 v[130:131], v[114:115], v[130:131] op_sel_hi:[0,1]
	v_pk_mul_f32 v[132:133], v[8:9], v[116:117]
	v_pk_mul_f32 v[134:135], v[10:11], v[118:119]
	v_pk_mul_f32 v[136:137], v[12:13], v[120:121]
	v_pk_mul_f32 v[138:139], v[14:15], v[122:123]
	v_pk_mul_f32 v[140:141], v[16:17], v[124:125]
	v_pk_mul_f32 v[142:143], v[18:19], v[126:127]
	v_pk_mul_f32 v[144:145], v[20:21], v[128:129]
	v_pk_mul_f32 v[146:147], v[22:23], v[130:131]
	global_store_dwordx4 v2, v[132:135], s[36:37] offset:0 sc1
	global_store_dwordx4 v2, v[136:139], s[36:37] offset:1024 sc1
	global_store_dwordx4 v2, v[140:143], s[36:37] offset:2048 sc1
	global_store_dwordx4 v2, v[144:147], s[36:37] offset:3072 sc1
	s_waitcnt vmcnt(33)
	v_add_f32_dpp v112, v60, v60 quad_perm:[1,0,3,2] row_mask:0xf bank_mask:0xf
	s_mov_b64 s[34:35], s[24:25]
	s_add_u32 s24, s24, s22
	v_add_f32_dpp v112, v112, v112 quad_perm:[2,3,0,1] row_mask:0xf bank_mask:0xf
	s_addc_u32 s25, s25, 0
	s_nop 0
	v_add_f32_dpp v112, v112, v112 row_half_mirror row_mask:0xf bank_mask:0xf
	s_nop 1
	v_add_f32_dpp v112, v112, v112 row_mirror row_mask:0xf bank_mask:0xf
	v_fmamk_f32 v112, v112, 0x3a800000, v5
	v_rsq_f32_e32 v114, v112
	v_lshlrev_b32_e32 v116, 16, v52
	v_and_b32_e32 v117, 0xffff0000, v52
	v_lshlrev_b32_e32 v118, 16, v53
	v_and_b32_e32 v119, 0xffff0000, v53
	v_lshlrev_b32_e32 v120, 16, v54
	v_and_b32_e32 v121, 0xffff0000, v54
	v_lshlrev_b32_e32 v122, 16, v55
	v_and_b32_e32 v123, 0xffff0000, v55
	v_lshlrev_b32_e32 v124, 16, v56
	v_and_b32_e32 v125, 0xffff0000, v56
	v_lshlrev_b32_e32 v126, 16, v57
	v_and_b32_e32 v127, 0xffff0000, v57
	v_lshlrev_b32_e32 v128, 16, v58
	v_and_b32_e32 v129, 0xffff0000, v58
	v_lshlrev_b32_e32 v130, 16, v59
	v_and_b32_e32 v131, 0xffff0000, v59
	v_pk_mul_f32 v[116:117], v[114:115], v[116:117] op_sel_hi:[0,1]
	v_pk_mul_f32 v[118:119], v[114:115], v[118:119] op_sel_hi:[0,1]
	v_pk_mul_f32 v[120:121], v[114:115], v[120:121] op_sel_hi:[0,1]
	v_pk_mul_f32 v[122:123], v[114:115], v[122:123] op_sel_hi:[0,1]
	v_pk_mul_f32 v[124:125], v[114:115], v[124:125] op_sel_hi:[0,1]
	v_pk_mul_f32 v[126:127], v[114:115], v[126:127] op_sel_hi:[0,1]
	v_pk_mul_f32 v[128:129], v[114:115], v[128:129] op_sel_hi:[0,1]
	v_pk_mul_f32 v[130:131], v[114:115], v[130:131] op_sel_hi:[0,1]
	v_pk_mul_f32 v[132:133], v[8:9], v[116:117]
	v_pk_mul_f32 v[134:135], v[10:11], v[118:119]
	v_pk_mul_f32 v[136:137], v[12:13], v[120:121]
	v_pk_mul_f32 v[138:139], v[14:15], v[122:123]
	v_pk_mul_f32 v[140:141], v[16:17], v[124:125]
	v_pk_mul_f32 v[142:143], v[18:19], v[126:127]
	v_pk_mul_f32 v[144:145], v[20:21], v[128:129]
	v_pk_mul_f32 v[146:147], v[22:23], v[130:131]
	global_store_dwordx4 v2, v[132:135], s[34:35] offset:0 sc1
	global_store_dwordx4 v2, v[136:139], s[34:35] offset:1024 sc1
	global_store_dwordx4 v2, v[140:143], s[34:35] offset:2048 sc1
	global_store_dwordx4 v2, v[144:147], s[34:35] offset:3072 sc1
	s_waitcnt vmcnt(32)
	v_add_f32_dpp v112, v70, v70 quad_perm:[1,0,3,2] row_mask:0xf bank_mask:0xf
	s_mov_b64 s[36:37], s[24:25]
	s_add_u32 s24, s24, s22
	v_add_f32_dpp v112, v112, v112 quad_perm:[2,3,0,1] row_mask:0xf bank_mask:0xf
	s_addc_u32 s25, s25, 0
	s_nop 0
	v_add_f32_dpp v112, v112, v112 row_half_mirror row_mask:0xf bank_mask:0xf
	s_nop 1
	v_add_f32_dpp v112, v112, v112 row_mirror row_mask:0xf bank_mask:0xf
	v_fmamk_f32 v112, v112, 0x3a800000, v5
	v_rsq_f32_e32 v114, v112
	v_lshlrev_b32_e32 v116, 16, v62
	v_and_b32_e32 v117, 0xffff0000, v62
	v_lshlrev_b32_e32 v118, 16, v63
	v_and_b32_e32 v119, 0xffff0000, v63
	v_lshlrev_b32_e32 v120, 16, v64
	v_and_b32_e32 v121, 0xffff0000, v64
	v_lshlrev_b32_e32 v122, 16, v65
	v_and_b32_e32 v123, 0xffff0000, v65
	v_lshlrev_b32_e32 v124, 16, v66
	v_and_b32_e32 v125, 0xffff0000, v66
	v_lshlrev_b32_e32 v126, 16, v67
	v_and_b32_e32 v127, 0xffff0000, v67
	v_lshlrev_b32_e32 v128, 16, v68
	v_and_b32_e32 v129, 0xffff0000, v68
	v_lshlrev_b32_e32 v130, 16, v69
	v_and_b32_e32 v131, 0xffff0000, v69
	v_pk_mul_f32 v[116:117], v[114:115], v[116:117] op_sel_hi:[0,1]
	v_pk_mul_f32 v[118:119], v[114:115], v[118:119] op_sel_hi:[0,1]
	v_pk_mul_f32 v[120:121], v[114:115], v[120:121] op_sel_hi:[0,1]
	v_pk_mul_f32 v[122:123], v[114:115], v[122:123] op_sel_hi:[0,1]
	v_pk_mul_f32 v[124:125], v[114:115], v[124:125] op_sel_hi:[0,1]
	v_pk_mul_f32 v[126:127], v[114:115], v[126:127] op_sel_hi:[0,1]
	v_pk_mul_f32 v[128:129], v[114:115], v[128:129] op_sel_hi:[0,1]
	v_pk_mul_f32 v[130:131], v[114:115], v[130:131] op_sel_hi:[0,1]
	v_pk_mul_f32 v[132:133], v[8:9], v[116:117]
	v_pk_mul_f32 v[134:135], v[10:11], v[118:119]
	v_pk_mul_f32 v[136:137], v[12:13], v[120:121]
	v_pk_mul_f32 v[138:139], v[14:15], v[122:123]
	v_pk_mul_f32 v[140:141], v[16:17], v[124:125]
	v_pk_mul_f32 v[142:143], v[18:19], v[126:127]
	v_pk_mul_f32 v[144:145], v[20:21], v[128:129]
	v_pk_mul_f32 v[146:147], v[22:23], v[130:131]
	global_store_dwordx4 v2, v[132:135], s[36:37] offset:0 sc1
	global_store_dwordx4 v2, v[136:139], s[36:37] offset:1024 sc1
	global_store_dwordx4 v2, v[140:143], s[36:37] offset:2048 sc1
	global_store_dwordx4 v2, v[144:147], s[36:37] offset:3072 sc1
.Lfin_loop:
	s_add_i32 s14, s12, s23
	s_cmp_lt_i32 s14, 0x10000
	s_cbranch_scc0 .Lfin_drain
	s_mov_b64 s[26:27], s[16:17]
	s_mov_b64 s[28:29], s[18:19]
	global_load_dword v40, v4, s[26:27]
	global_load_dwordx2 v[32:33], v3, s[28:29] offset:0 nt
	global_load_dwordx2 v[34:35], v3, s[28:29] offset:512 nt
	global_load_dwordx2 v[36:37], v3, s[28:29] offset:1024 nt
	global_load_dwordx2 v[38:39], v3, s[28:29] offset:1536 nt
	s_add_u32 s16, s16, s20
	s_addc_u32 s17, s17, 0
	s_add_u32 s18, s18, s21
	s_addc_u32 s19, s19, 0
	s_add_i32 s12, s12, s13
	s_mov_b64 s[30:31], s[16:17]
	s_mov_b64 s[32:33], s[18:19]
	global_load_dword v50, v4, s[30:31]
	global_load_dwordx2 v[42:43], v3, s[32:33] offset:0 nt
	global_load_dwordx2 v[44:45], v3, s[32:33] offset:512 nt
	global_load_dwordx2 v[46:47], v3, s[32:33] offset:1024 nt
	global_load_dwordx2 v[48:49], v3, s[32:33] offset:1536 nt
	s_add_u32 s16, s16, s20
	s_addc_u32 s17, s17, 0
	s_add_u32 s18, s18, s21
	s_addc_u32 s19, s19, 0
	s_add_i32 s12, s12, s13
	s_mov_b64 s[26:27], s[16:17]
	s_mov_b64 s[28:29], s[18:19]
	global_load_dword v60, v4, s[26:27]
	global_load_dwordx2 v[52:53], v3, s[28:29] offset:0 nt
	global_load_dwordx2 v[54:55], v3, s[28:29] offset:512 nt
	global_load_dwordx2 v[56:57], v3, s[28:29] offset:1024 nt
	global_load_dwordx2 v[58:59], v3, s[28:29] offset:1536 nt
	s_add_u32 s16, s16, s20
	s_addc_u32 s17, s17, 0
	s_add_u32 s18, s18, s21
	s_addc_u32 s19, s19, 0
	s_add_i32 s12, s12, s13
	s_mov_b64 s[30:31], s[16:17]
	s_mov_b64 s[32:33], s[18:19]
	global_load_dword v70, v4, s[30:31]
	global_load_dwordx2 v[62:63], v3, s[32:33] offset:0 nt
	global_load_dwordx2 v[64:65], v3, s[32:33] offset:512 nt
	global_load_dwordx2 v[66:67], v3, s[32:33] offset:1024 nt
	global_load_dwordx2 v[68:69], v3, s[32:33] offset:1536 nt
	s_add_u32 s16, s16, s20
	s_addc_u32 s17, s17, 0
	s_add_u32 s18, s18, s21
	s_addc_u32 s19, s19, 0
	s_add_i32 s12, s12, s13
	s_waitcnt vmcnt(51)
	v_add_f32_dpp v112, v80, v80 quad_perm:[1,0,3,2] row_mask:0xf bank_mask:0xf
	s_mov_b64 s[34:35], s[24:25]
	s_add_u32 s24, s24, s22
	v_add_f32_dpp v112, v112, v112 quad_perm:[2,3,0,1] row_mask:0xf bank_mask:0xf
	s_addc_u32 s25, s25, 0
	s_nop 0
	v_add_f32_dpp v112, v112, v112 row_half_mirror row_mask:0xf bank_mask:0xf
	s_nop 1
	v_add_f32_dpp v112, v112, v112 row_mirror row_mask:0xf bank_mask:0xf
	v_fmamk_f32 v112, v112, 0x3a800000, v5
	v_rsq_f32_e32 v114, v112
	v_lshlrev_b32_e32 v116, 16, v72
	v_and_b32_e32 v117, 0xffff0000, v72
	v_lshlrev_b32_e32 v118, 16, v73
	v_and_b32_e32 v119, 0xffff0000, v73
	v_lshlrev_b32_e32 v120, 16, v74
	v_and_b32_e32 v121, 0xffff0000, v74
	v_lshlrev_b32_e32 v122, 16, v75
	v_and_b32_e32 v123, 0xffff0000, v75
	v_lshlrev_b32_e32 v124, 16, v76
	v_and_b32_e32 v125, 0xffff0000, v76
	v_lshlrev_b32_e32 v126, 16, v77
	v_and_b32_e32 v127, 0xffff0000, v77
	v_lshlrev_b32_e32 v128, 16, v78
	v_and_b32_e32 v129, 0xffff0000, v78
	v_lshlrev_b32_e32 v130, 16, v79
	v_and_b32_e32 v131, 0xffff0000, v79
	v_pk_mul_f32 v[116:117], v[114:115], v[116:117] op_sel_hi:[0,1]
	v_pk_mul_f32 v[118:119], v[114:115], v[118:119] op_sel_hi:[0,1]
	v_pk_mul_f32 v[120:121], v[114:115], v[120:121] op_sel_hi:[0,1]
	v_pk_mul_f32 v[122:123], v[114:115], v[122:123] op_sel_hi:[0,1]
	v_pk_mul_f32 v[124:125], v[114:115], v[124:125] op_sel_hi:[0,1]
	v_pk_mul_f32 v[126:127], v[114:115], v[126:127] op_sel_hi:[0,1]
	v_pk_mul_f32 v[128:129], v[114:115], v[128:129] op_sel_hi:[0,1]
	v_pk_mul_f32 v[130:131], v[114:115], v[130:131] op_sel_hi:[0,1]
	v_pk_mul_f32 v[132:133], v[8:9], v[116:117]
	v_pk_mul_f32 v[134:135], v[10:11], v[118:119]
	v_pk_mul_f32 v[136:137], v[12:13], v[120:121]
	v_pk_mul_f32 v[138:139], v[14:15], v[122:123]
	v_pk_mul_f32 v[140:141], v[16:17], v[124:125]
	v_pk_mul_f32 v[142:143], v[18:19], v[126:127]
	v_pk_mul_f32 v[144:145], v[20:21], v[128:129]
	v_pk_mul_f32 v[146:147], v[22:23], v[130:131]
	global_store_dwordx4 v2, v[132:135], s[34:35] offset:0 sc1
	global_store_dwordx4 v2, v[136:139], s[34:35] offset:1024 sc1
	global_store_dwordx4 v2, v[140:143], s[34:35] offset:2048 sc1
	global_store_dwordx4 v2, v[144:147], s[34:35] offset:3072 sc1
	s_waitcnt vmcnt(50)
	v_add_f32_dpp v112, v90, v90 quad_perm:[1,0,3,2] row_mask:0xf bank_mask:0xf
	s_mov_b64 s[36:37], s[24:25]
	s_add_u32 s24, s24, s22
	v_add_f32_dpp v112, v112, v112 quad_perm:[2,3,0,1] row_mask:0xf bank_mask:0xf
	s_addc_u32 s25, s25, 0
	s_nop 0
	v_add_f32_dpp v112, v112, v112 row_half_mirror row_mask:0xf bank_mask:0xf
	s_nop 1
	v_add_f32_dpp v112, v112, v112 row_mirror row_mask:0xf bank_mask:0xf
	v_fmamk_f32 v112, v112, 0x3a800000, v5
	v_rsq_f32_e32 v114, v112
	v_lshlrev_b32_e32 v116, 16, v82
	v_and_b32_e32 v117, 0xffff0000, v82
	v_lshlrev_b32_e32 v118, 16, v83
	v_and_b32_e32 v119, 0xffff0000, v83
	v_lshlrev_b32_e32 v120, 16, v84
	v_and_b32_e32 v121, 0xffff0000, v84
	v_lshlrev_b32_e32 v122, 16, v85
	v_and_b32_e32 v123, 0xffff0000, v85
	v_lshlrev_b32_e32 v124, 16, v86
	v_and_b32_e32 v125, 0xffff0000, v86
	v_lshlrev_b32_e32 v126, 16, v87
	v_and_b32_e32 v127, 0xffff0000, v87
	v_lshlrev_b32_e32 v128, 16, v88
	v_and_b32_e32 v129, 0xffff0000, v88
	v_lshlrev_b32_e32 v130, 16, v89
	v_and_b32_e32 v131, 0xffff0000, v89
	v_pk_mul_f32 v[116:117], v[114:115], v[116:117] op_sel_hi:[0,1]
	v_pk_mul_f32 v[118:119], v[114:115], v[118:119] op_sel_hi:[0,1]
	v_pk_mul_f32 v[120:121], v[114:115], v[120:121] op_sel_hi:[0,1]
	v_pk_mul_f32 v[122:123], v[114:115], v[122:123] op_sel_hi:[0,1]
	v_pk_mul_f32 v[124:125], v[114:115], v[124:125] op_sel_hi:[0,1]
	v_pk_mul_f32 v[126:127], v[114:115], v[126:127] op_sel_hi:[0,1]
	v_pk_mul_f32 v[128:129], v[114:115], v[128:129] op_sel_hi:[0,1]
	v_pk_mul_f32 v[130:131], v[114:115], v[130:131] op_sel_hi:[0,1]
	v_pk_mul_f32 v[132:133], v[8:9], v[116:117]
	v_pk_mul_f32 v[134:135], v[10:11], v[118:119]
	v_pk_mul_f32 v[136:137], v[12:13], v[120:121]
	v_pk_mul_f32 v[138:139], v[14:15], v[122:123]
	v_pk_mul_f32 v[140:141], v[16:17], v[124:125]
	v_pk_mul_f32 v[142:143], v[18:19], v[126:127]
	v_pk_mul_f32 v[144:145], v[20:21], v[128:129]
	v_pk_mul_f32 v[146:147], v[22:23], v[130:131]
	global_store_dwordx4 v2, v[132:135], s[36:37] offset:0 sc1
	global_store_dwordx4 v2, v[136:139], s[36:37] offset:1024 sc1
	global_store_dwordx4 v2, v[140:143], s[36:37] offset:2048 sc1
	global_store_dwordx4 v2, v[144:147], s[36:37] offset:3072 sc1
	s_waitcnt vmcnt(49)
	v_add_f32_dpp v112, v100, v100 quad_perm:[1,0,3,2] row_mask:0xf bank_mask:0xf
	s_mov_b64 s[34:35], s[24:25]
	s_add_u32 s24, s24, s22
	v_add_f32_dpp v112, v112, v112 quad_perm:[2,3,0,1] row_mask:0xf bank_mask:0xf
	s_addc_u32 s25, s25, 0
	s_nop 0
	v_add_f32_dpp v112, v112, v112 row_half_mirror row_mask:0xf bank_mask:0xf
	s_nop 1
	v_add_f32_dpp v112, v112, v112 row_mirror row_mask:0xf bank_mask:0xf
	v_fmamk_f32 v112, v112, 0x3a800000, v5
	v_rsq_f32_e32 v114, v112
	v_lshlrev_b32_e32 v116, 16, v92
	v_and_b32_e32 v117, 0xffff0000, v92
	v_lshlrev_b32_e32 v118, 16, v93
	v_and_b32_e32 v119, 0xffff0000, v93
	v_lshlrev_b32_e32 v120, 16, v94
	v_and_b32_e32 v121, 0xffff0000, v94
	v_lshlrev_b32_e32 v122, 16, v95
	v_and_b32_e32 v123, 0xffff0000, v95
	v_lshlrev_b32_e32 v124, 16, v96
	v_and_b32_e32 v125, 0xffff0000, v96
	v_lshlrev_b32_e32 v126, 16, v97
	v_and_b32_e32 v127, 0xffff0000, v97
	v_lshlrev_b32_e32 v128, 16, v98
	v_and_b32_e32 v129, 0xffff0000, v98
	v_lshlrev_b32_e32 v130, 16, v99
	v_and_b32_e32 v131, 0xffff0000, v99
	v_pk_mul_f32 v[116:117], v[114:115], v[116:117] op_sel_hi:[0,1]
	v_pk_mul_f32 v[118:119], v[114:115], v[118:119] op_sel_hi:[0,1]
	v_pk_mul_f32 v[120:121], v[114:115], v[120:121] op_sel_hi:[0,1]
	v_pk_mul_f32 v[122:123], v[114:115], v[122:123] op_sel_hi:[0,1]
	v_pk_mul_f32 v[124:125], v[114:115], v[124:125] op_sel_hi:[0,1]
	v_pk_mul_f32 v[126:127], v[114:115], v[126:127] op_sel_hi:[0,1]
	v_pk_mul_f32 v[128:129], v[114:115], v[128:129] op_sel_hi:[0,1]
	v_pk_mul_f32 v[130:131], v[114:115], v[130:131] op_sel_hi:[0,1]
	v_pk_mul_f32 v[132:133], v[8:9], v[116:117]
	v_pk_mul_f32 v[134:135], v[10:11], v[118:119]
	v_pk_mul_f32 v[136:137], v[12:13], v[120:121]
	v_pk_mul_f32 v[138:139], v[14:15], v[122:123]
	v_pk_mul_f32 v[140:141], v[16:17], v[124:125]
	v_pk_mul_f32 v[142:143], v[18:19], v[126:127]
	v_pk_mul_f32 v[144:145], v[20:21], v[128:129]
	v_pk_mul_f32 v[146:147], v[22:23], v[130:131]
	global_store_dwordx4 v2, v[132:135], s[34:35] offset:0 sc1
	global_store_dwordx4 v2, v[136:139], s[34:35] offset:1024 sc1
	global_store_dwordx4 v2, v[140:143], s[34:35] offset:2048 sc1
	global_store_dwordx4 v2, v[144:147], s[34:35] offset:3072 sc1
	s_waitcnt vmcnt(48)
	v_add_f32_dpp v112, v110, v110 quad_perm:[1,0,3,2] row_mask:0xf bank_mask:0xf
	s_mov_b64 s[36:37], s[24:25]
	s_add_u32 s24, s24, s22
	v_add_f32_dpp v112, v112, v112 quad_perm:[2,3,0,1] row_mask:0xf bank_mask:0xf
	s_addc_u32 s25, s25, 0
	s_nop 0
	v_add_f32_dpp v112, v112, v112 row_half_mirror row_mask:0xf bank_mask:0xf
	s_nop 1
	v_add_f32_dpp v112, v112, v112 row_mirror row_mask:0xf bank_mask:0xf
	v_fmamk_f32 v112, v112, 0x3a800000, v5
	v_rsq_f32_e32 v114, v112
	v_lshlrev_b32_e32 v116, 16, v102
	v_and_b32_e32 v117, 0xffff0000, v102
	v_lshlrev_b32_e32 v118, 16, v103
	v_and_b32_e32 v119, 0xffff0000, v103
	v_lshlrev_b32_e32 v120, 16, v104
	v_and_b32_e32 v121, 0xffff0000, v104
	v_lshlrev_b32_e32 v122, 16, v105
	v_and_b32_e32 v123, 0xffff0000, v105
	v_lshlrev_b32_e32 v124, 16, v106
	v_and_b32_e32 v125, 0xffff0000, v106
	v_lshlrev_b32_e32 v126, 16, v107
	v_and_b32_e32 v127, 0xffff0000, v107
	v_lshlrev_b32_e32 v128, 16, v108
	v_and_b32_e32 v129, 0xffff0000, v108
	v_lshlrev_b32_e32 v130, 16, v109
	v_and_b32_e32 v131, 0xffff0000, v109
	v_pk_mul_f32 v[116:117], v[114:115], v[116:117] op_sel_hi:[0,1]
	v_pk_mul_f32 v[118:119], v[114:115], v[118:119] op_sel_hi:[0,1]
	v_pk_mul_f32 v[120:121], v[114:115], v[120:121] op_sel_hi:[0,1]
	v_pk_mul_f32 v[122:123], v[114:115], v[122:123] op_sel_hi:[0,1]
	v_pk_mul_f32 v[124:125], v[114:115], v[124:125] op_sel_hi:[0,1]
	v_pk_mul_f32 v[126:127], v[114:115], v[126:127] op_sel_hi:[0,1]
	v_pk_mul_f32 v[128:129], v[114:115], v[128:129] op_sel_hi:[0,1]
	v_pk_mul_f32 v[130:131], v[114:115], v[130:131] op_sel_hi:[0,1]
	v_pk_mul_f32 v[132:133], v[8:9], v[116:117]
	v_pk_mul_f32 v[134:135], v[10:11], v[118:119]
	v_pk_mul_f32 v[136:137], v[12:13], v[120:121]
	v_pk_mul_f32 v[138:139], v[14:15], v[122:123]
	v_pk_mul_f32 v[140:141], v[16:17], v[124:125]
	v_pk_mul_f32 v[142:143], v[18:19], v[126:127]
	v_pk_mul_f32 v[144:145], v[20:21], v[128:129]
	v_pk_mul_f32 v[146:147], v[22:23], v[130:131]
	global_store_dwordx4 v2, v[132:135], s[36:37] offset:0 sc1
	global_store_dwordx4 v2, v[136:139], s[36:37] offset:1024 sc1
	global_store_dwordx4 v2, v[140:143], s[36:37] offset:2048 sc1
	global_store_dwordx4 v2, v[144:147], s[36:37] offset:3072 sc1
	s_mov_b64 s[26:27], s[16:17]
	s_mov_b64 s[28:29], s[18:19]
	global_load_dword v80, v4, s[26:27]
	global_load_dwordx2 v[72:73], v3, s[28:29] offset:0 nt
	global_load_dwordx2 v[74:75], v3, s[28:29] offset:512 nt
	global_load_dwordx2 v[76:77], v3, s[28:29] offset:1024 nt
	global_load_dwordx2 v[78:79], v3, s[28:29] offset:1536 nt
	s_add_u32 s16, s16, s20
	s_addc_u32 s17, s17, 0
	s_add_u32 s18, s18, s21
	s_addc_u32 s19, s19, 0
	s_add_i32 s12, s12, s13
	s_mov_b64 s[30:31], s[16:17]
	s_mov_b64 s[32:33], s[18:19]
	global_load_dword v90, v4, s[30:31]
	global_load_dwordx2 v[82:83], v3, s[32:33] offset:0 nt
	global_load_dwordx2 v[84:85], v3, s[32:33] offset:512 nt
	global_load_dwordx2 v[86:87], v3, s[32:33] offset:1024 nt
	global_load_dwordx2 v[88:89], v3, s[32:33] offset:1536 nt
	s_add_u32 s16, s16, s20
	s_addc_u32 s17, s17, 0
	s_add_u32 s18, s18, s21
	s_addc_u32 s19, s19, 0
	s_add_i32 s12, s12, s13
	s_mov_b64 s[26:27], s[16:17]
	s_mov_b64 s[28:29], s[18:19]
	global_load_dword v100, v4, s[26:27]
	global_load_dwordx2 v[92:93], v3, s[28:29] offset:0 nt
	global_load_dwordx2 v[94:95], v3, s[28:29] offset:512 nt
	global_load_dwordx2 v[96:97], v3, s[28:29] offset:1024 nt
	global_load_dwordx2 v[98:99], v3, s[28:29] offset:1536 nt
	s_add_u32 s16, s16, s20
	s_addc_u32 s17, s17, 0
	s_add_u32 s18, s18, s21
	s_addc_u32 s19, s19, 0
	s_add_i32 s12, s12, s13
	s_mov_b64 s[30:31], s[16:17]
	s_mov_b64 s[32:33], s[18:19]
	global_load_dword v110, v4, s[30:31]
	global_load_dwordx2 v[102:103], v3, s[32:33] offset:0 nt
	global_load_dwordx2 v[104:105], v3, s[32:33] offset:512 nt
	global_load_dwordx2 v[106:107], v3, s[32:33] offset:1024 nt
	global_load_dwordx2 v[108:109], v3, s[32:33] offset:1536 nt
	s_add_u32 s16, s16, s20
	s_addc_u32 s17, s17, 0
	s_add_u32 s18, s18, s21
	s_addc_u32 s19, s19, 0
	s_add_i32 s12, s12, s13
	s_waitcnt vmcnt(51)
	v_add_f32_dpp v112, v40, v40 quad_perm:[1,0,3,2] row_mask:0xf bank_mask:0xf
	s_mov_b64 s[34:35], s[24:25]
	s_add_u32 s24, s24, s22
	v_add_f32_dpp v112, v112, v112 quad_perm:[2,3,0,1] row_mask:0xf bank_mask:0xf
	s_addc_u32 s25, s25, 0
	s_nop 0
	v_add_f32_dpp v112, v112, v112 row_half_mirror row_mask:0xf bank_mask:0xf
	s_nop 1
	v_add_f32_dpp v112, v112, v112 row_mirror row_mask:0xf bank_mask:0xf
	v_fmamk_f32 v112, v112, 0x3a800000, v5
	v_rsq_f32_e32 v114, v112
	v_lshlrev_b32_e32 v116, 16, v32
	v_and_b32_e32 v117, 0xffff0000, v32
	v_lshlrev_b32_e32 v118, 16, v33
	v_and_b32_e32 v119, 0xffff0000, v33
	v_lshlrev_b32_e32 v120, 16, v34
	v_and_b32_e32 v121, 0xffff0000, v34
	v_lshlrev_b32_e32 v122, 16, v35
	v_and_b32_e32 v123, 0xffff0000, v35
	v_lshlrev_b32_e32 v124, 16, v36
	v_and_b32_e32 v125, 0xffff0000, v36
	v_lshlrev_b32_e32 v126, 16, v37
	v_and_b32_e32 v127, 0xffff0000, v37
	v_lshlrev_b32_e32 v128, 16, v38
	v_and_b32_e32 v129, 0xffff0000, v38
	v_lshlrev_b32_e32 v130, 16, v39
	v_and_b32_e32 v131, 0xffff0000, v39
	v_pk_mul_f32 v[116:117], v[114:115], v[116:117] op_sel_hi:[0,1]
	v_pk_mul_f32 v[118:119], v[114:115], v[118:119] op_sel_hi:[0,1]
	v_pk_mul_f32 v[120:121], v[114:115], v[120:121] op_sel_hi:[0,1]
	v_pk_mul_f32 v[122:123], v[114:115], v[122:123] op_sel_hi:[0,1]
	v_pk_mul_f32 v[124:125], v[114:115], v[124:125] op_sel_hi:[0,1]
	v_pk_mul_f32 v[126:127], v[114:115], v[126:127] op_sel_hi:[0,1]
	v_pk_mul_f32 v[128:129], v[114:115], v[128:129] op_sel_hi:[0,1]
	v_pk_mul_f32 v[130:131], v[114:115], v[130:131] op_sel_hi:[0,1]
	v_pk_mul_f32 v[132:133], v[8:9], v[116:117]
	v_pk_mul_f32 v[134:135], v[10:11], v[118:119]
	v_pk_mul_f32 v[136:137], v[12:13], v[120:121]
	v_pk_mul_f32 v[138:139], v[14:15], v[122:123]
	v_pk_mul_f32 v[140:141], v[16:17], v[124:125]
	v_pk_mul_f32 v[142:143], v[18:19], v[126:127]
	v_pk_mul_f32 v[144:145], v[20:21], v[128:129]
	v_pk_mul_f32 v[146:147], v[22:23], v[130:131]
	global_store_dwordx4 v2, v[132:135], s[34:35] offset:0 sc1
	global_store_dwordx4 v2, v[136:139], s[34:35] offset:1024 sc1
	global_store_dwordx4 v2, v[140:143], s[34:35] offset:2048 sc1
	global_store_dwordx4 v2, v[144:147], s[34:35] offset:3072 sc1
	s_waitcnt vmcnt(50)
	v_add_f32_dpp v112, v50, v50 quad_perm:[1,0,3,2] row_mask:0xf bank_mask:0xf
	s_mov_b64 s[36:37], s[24:25]
	s_add_u32 s24, s24, s22
	v_add_f32_dpp v112, v112, v112 quad_perm:[2,3,0,1] row_mask:0xf bank_mask:0xf
	s_addc_u32 s25, s25, 0
	s_nop 0
	v_add_f32_dpp v112, v112, v112 row_half_mirror row_mask:0xf bank_mask:0xf
	s_nop 1
	v_add_f32_dpp v112, v112, v112 row_mirror row_mask:0xf bank_mask:0xf
	v_fmamk_f32 v112, v112, 0x3a800000, v5
	v_rsq_f32_e32 v114, v112
	v_lshlrev_b32_e32 v116, 16, v42
	v_and_b32_e32 v117, 0xffff0000, v42
	v_lshlrev_b32_e32 v118, 16, v43
	v_and_b32_e32 v119, 0xffff0000, v43
	v_lshlrev_b32_e32 v120, 16, v44
	v_and_b32_e32 v121, 0xffff0000, v44
	v_lshlrev_b32_e32 v122, 16, v45
	v_and_b32_e32 v123, 0xffff0000, v45
	v_lshlrev_b32_e32 v124, 16, v46
	v_and_b32_e32 v125, 0xffff0000, v46
	v_lshlrev_b32_e32 v126, 16, v47
	v_and_b32_e32 v127, 0xffff0000, v47
	v_lshlrev_b32_e32 v128, 16, v48
	v_and_b32_e32 v129, 0xffff0000, v48
	v_lshlrev_b32_e32 v130, 16, v49
	v_and_b32_e32 v131, 0xffff0000, v49
	v_pk_mul_f32 v[116:117], v[114:115], v[116:117] op_sel_hi:[0,1]
	v_pk_mul_f32 v[118:119], v[114:115], v[118:119] op_sel_hi:[0,1]
	v_pk_mul_f32 v[120:121], v[114:115], v[120:121] op_sel_hi:[0,1]
	v_pk_mul_f32 v[122:123], v[114:115], v[122:123] op_sel_hi:[0,1]
	v_pk_mul_f32 v[124:125], v[114:115], v[124:125] op_sel_hi:[0,1]
	v_pk_mul_f32 v[126:127], v[114:115], v[126:127] op_sel_hi:[0,1]
	v_pk_mul_f32 v[128:129], v[114:115], v[128:129] op_sel_hi:[0,1]
	v_pk_mul_f32 v[130:131], v[114:115], v[130:131] op_sel_hi:[0,1]
	v_pk_mul_f32 v[132:133], v[8:9], v[116:117]
	v_pk_mul_f32 v[134:135], v[10:11], v[118:119]
	v_pk_mul_f32 v[136:137], v[12:13], v[120:121]
	v_pk_mul_f32 v[138:139], v[14:15], v[122:123]
	v_pk_mul_f32 v[140:141], v[16:17], v[124:125]
	v_pk_mul_f32 v[142:143], v[18:19], v[126:127]
	v_pk_mul_f32 v[144:145], v[20:21], v[128:129]
	v_pk_mul_f32 v[146:147], v[22:23], v[130:131]
	global_store_dwordx4 v2, v[132:135], s[36:37] offset:0 sc1
	global_store_dwordx4 v2, v[136:139], s[36:37] offset:1024 sc1
	global_store_dwordx4 v2, v[140:143], s[36:37] offset:2048 sc1
	global_store_dwordx4 v2, v[144:147], s[36:37] offset:3072 sc1
	s_waitcnt vmcnt(49)
	v_add_f32_dpp v112, v60, v60 quad_perm:[1,0,3,2] row_mask:0xf bank_mask:0xf
	s_mov_b64 s[34:35], s[24:25]
	s_add_u32 s24, s24, s22
	v_add_f32_dpp v112, v112, v112 quad_perm:[2,3,0,1] row_mask:0xf bank_mask:0xf
	s_addc_u32 s25, s25, 0
	s_nop 0
	v_add_f32_dpp v112, v112, v112 row_half_mirror row_mask:0xf bank_mask:0xf
	s_nop 1
	v_add_f32_dpp v112, v112, v112 row_mirror row_mask:0xf bank_mask:0xf
	v_fmamk_f32 v112, v112, 0x3a800000, v5
	v_rsq_f32_e32 v114, v112
	v_lshlrev_b32_e32 v116, 16, v52
	v_and_b32_e32 v117, 0xffff0000, v52
	v_lshlrev_b32_e32 v118, 16, v53
	v_and_b32_e32 v119, 0xffff0000, v53
	v_lshlrev_b32_e32 v120, 16, v54
	v_and_b32_e32 v121, 0xffff0000, v54
	v_lshlrev_b32_e32 v122, 16, v55
	v_and_b32_e32 v123, 0xffff0000, v55
	v_lshlrev_b32_e32 v124, 16, v56
	v_and_b32_e32 v125, 0xffff0000, v56
	v_lshlrev_b32_e32 v126, 16, v57
	v_and_b32_e32 v127, 0xffff0000, v57
	v_lshlrev_b32_e32 v128, 16, v58
	v_and_b32_e32 v129, 0xffff0000, v58
	v_lshlrev_b32_e32 v130, 16, v59
	v_and_b32_e32 v131, 0xffff0000, v59
	v_pk_mul_f32 v[116:117], v[114:115], v[116:117] op_sel_hi:[0,1]
	v_pk_mul_f32 v[118:119], v[114:115], v[118:119] op_sel_hi:[0,1]
	v_pk_mul_f32 v[120:121], v[114:115], v[120:121] op_sel_hi:[0,1]
	v_pk_mul_f32 v[122:123], v[114:115], v[122:123] op_sel_hi:[0,1]
	v_pk_mul_f32 v[124:125], v[114:115], v[124:125] op_sel_hi:[0,1]
	v_pk_mul_f32 v[126:127], v[114:115], v[126:127] op_sel_hi:[0,1]
	v_pk_mul_f32 v[128:129], v[114:115], v[128:129] op_sel_hi:[0,1]
	v_pk_mul_f32 v[130:131], v[114:115], v[130:131] op_sel_hi:[0,1]
	v_pk_mul_f32 v[132:133], v[8:9], v[116:117]
	v_pk_mul_f32 v[134:135], v[10:11], v[118:119]
	v_pk_mul_f32 v[136:137], v[12:13], v[120:121]
	v_pk_mul_f32 v[138:139], v[14:15], v[122:123]
	v_pk_mul_f32 v[140:141], v[16:17], v[124:125]
	v_pk_mul_f32 v[142:143], v[18:19], v[126:127]
	v_pk_mul_f32 v[144:145], v[20:21], v[128:129]
	v_pk_mul_f32 v[146:147], v[22:23], v[130:131]
	global_store_dwordx4 v2, v[132:135], s[34:35] offset:0 sc1
	global_store_dwordx4 v2, v[136:139], s[34:35] offset:1024 sc1
	global_store_dwordx4 v2, v[140:143], s[34:35] offset:2048 sc1
	global_store_dwordx4 v2, v[144:147], s[34:35] offset:3072 sc1
	s_waitcnt vmcnt(48)
	v_add_f32_dpp v112, v70, v70 quad_perm:[1,0,3,2] row_mask:0xf bank_mask:0xf
	s_mov_b64 s[36:37], s[24:25]
	s_add_u32 s24, s24, s22
	v_add_f32_dpp v112, v112, v112 quad_perm:[2,3,0,1] row_mask:0xf bank_mask:0xf
	s_addc_u32 s25, s25, 0
	s_nop 0
	v_add_f32_dpp v112, v112, v112 row_half_mirror row_mask:0xf bank_mask:0xf
	s_nop 1
	v_add_f32_dpp v112, v112, v112 row_mirror row_mask:0xf bank_mask:0xf
	v_fmamk_f32 v112, v112, 0x3a800000, v5
	v_rsq_f32_e32 v114, v112
	v_lshlrev_b32_e32 v116, 16, v62
	v_and_b32_e32 v117, 0xffff0000, v62
	v_lshlrev_b32_e32 v118, 16, v63
	v_and_b32_e32 v119, 0xffff0000, v63
	v_lshlrev_b32_e32 v120, 16, v64
	v_and_b32_e32 v121, 0xffff0000, v64
	v_lshlrev_b32_e32 v122, 16, v65
	v_and_b32_e32 v123, 0xffff0000, v65
	v_lshlrev_b32_e32 v124, 16, v66
	v_and_b32_e32 v125, 0xffff0000, v66
	v_lshlrev_b32_e32 v126, 16, v67
	v_and_b32_e32 v127, 0xffff0000, v67
	v_lshlrev_b32_e32 v128, 16, v68
	v_and_b32_e32 v129, 0xffff0000, v68
	v_lshlrev_b32_e32 v130, 16, v69
	v_and_b32_e32 v131, 0xffff0000, v69
	v_pk_mul_f32 v[116:117], v[114:115], v[116:117] op_sel_hi:[0,1]
	v_pk_mul_f32 v[118:119], v[114:115], v[118:119] op_sel_hi:[0,1]
	v_pk_mul_f32 v[120:121], v[114:115], v[120:121] op_sel_hi:[0,1]
	v_pk_mul_f32 v[122:123], v[114:115], v[122:123] op_sel_hi:[0,1]
	v_pk_mul_f32 v[124:125], v[114:115], v[124:125] op_sel_hi:[0,1]
	v_pk_mul_f32 v[126:127], v[114:115], v[126:127] op_sel_hi:[0,1]
	v_pk_mul_f32 v[128:129], v[114:115], v[128:129] op_sel_hi:[0,1]
	v_pk_mul_f32 v[130:131], v[114:115], v[130:131] op_sel_hi:[0,1]
	v_pk_mul_f32 v[132:133], v[8:9], v[116:117]
	v_pk_mul_f32 v[134:135], v[10:11], v[118:119]
	v_pk_mul_f32 v[136:137], v[12:13], v[120:121]
	v_pk_mul_f32 v[138:139], v[14:15], v[122:123]
	v_pk_mul_f32 v[140:141], v[16:17], v[124:125]
	v_pk_mul_f32 v[142:143], v[18:19], v[126:127]
	v_pk_mul_f32 v[144:145], v[20:21], v[128:129]
	v_pk_mul_f32 v[146:147], v[22:23], v[130:131]
	global_store_dwordx4 v2, v[132:135], s[36:37] offset:0 sc1
	global_store_dwordx4 v2, v[136:139], s[36:37] offset:1024 sc1
	global_store_dwordx4 v2, v[140:143], s[36:37] offset:2048 sc1
	global_store_dwordx4 v2, v[144:147], s[36:37] offset:3072 sc1
	s_branch .Lfin_loop

.Lfin_tail:
	s_cmp_lt_i32 s12, 0x10000
	s_cbranch_scc0 .LBB0_3641
	s_mov_b64 s[26:27], s[16:17]
	s_mov_b64 s[28:29], s[18:19]
	global_load_dword v40, v4, s[26:27]
	global_load_dwordx2 v[32:33], v3, s[28:29] offset:0 nt
	global_load_dwordx2 v[34:35], v3, s[28:29] offset:512 nt
	global_load_dwordx2 v[36:37], v3, s[28:29] offset:1024 nt
	global_load_dwordx2 v[38:39], v3, s[28:29] offset:1536 nt
	s_add_u32 s16, s16, s20
	s_addc_u32 s17, s17, 0
	s_add_u32 s18, s18, s21
	s_addc_u32 s19, s19, 0
	s_add_i32 s12, s12, s13
	s_waitcnt vmcnt(0)
	v_add_f32_dpp v112, v40, v40 quad_perm:[1,0,3,2] row_mask:0xf bank_mask:0xf
	s_mov_b64 s[34:35], s[24:25]
	s_add_u32 s24, s24, s22
	v_add_f32_dpp v112, v112, v112 quad_perm:[2,3,0,1] row_mask:0xf bank_mask:0xf
	s_addc_u32 s25, s25, 0
	s_nop 0
	v_add_f32_dpp v112, v112, v112 row_half_mirror row_mask:0xf bank_mask:0xf
	s_nop 1
	v_add_f32_dpp v112, v112, v112 row_mirror row_mask:0xf bank_mask:0xf
	v_fmamk_f32 v112, v112, 0x3a800000, v5
	v_rsq_f32_e32 v114, v112
	v_lshlrev_b32_e32 v116, 16, v32
	v_and_b32_e32 v117, 0xffff0000, v32
	v_lshlrev_b32_e32 v118, 16, v33
	v_and_b32_e32 v119, 0xffff0000, v33
	v_lshlrev_b32_e32 v120, 16, v34
	v_and_b32_e32 v121, 0xffff0000, v34
	v_lshlrev_b32_e32 v122, 16, v35
	v_and_b32_e32 v123, 0xffff0000, v35
	v_lshlrev_b32_e32 v124, 16, v36
	v_and_b32_e32 v125, 0xffff0000, v36
	v_lshlrev_b32_e32 v126, 16, v37
	v_and_b32_e32 v127, 0xffff0000, v37
	v_lshlrev_b32_e32 v128, 16, v38
	v_and_b32_e32 v129, 0xffff0000, v38
	v_lshlrev_b32_e32 v130, 16, v39
	v_and_b32_e32 v131, 0xffff0000, v39
	v_pk_mul_f32 v[116:117], v[114:115], v[116:117] op_sel_hi:[0,1]
	v_pk_mul_f32 v[118:119], v[114:115], v[118:119] op_sel_hi:[0,1]
	v_pk_mul_f32 v[120:121], v[114:115], v[120:121] op_sel_hi:[0,1]
	v_pk_mul_f32 v[122:123], v[114:115], v[122:123] op_sel_hi:[0,1]
	v_pk_mul_f32 v[124:125], v[114:115], v[124:125] op_sel_hi:[0,1]
	v_pk_mul_f32 v[126:127], v[114:115], v[126:127] op_sel_hi:[0,1]
	v_pk_mul_f32 v[128:129], v[114:115], v[128:129] op_sel_hi:[0,1]
	v_pk_mul_f32 v[130:131], v[114:115], v[130:131] op_sel_hi:[0,1]
	v_pk_mul_f32 v[132:133], v[8:9], v[116:117]
	v_pk_mul_f32 v[134:135], v[10:11], v[118:119]
	v_pk_mul_f32 v[136:137], v[12:13], v[120:121]
	v_pk_mul_f32 v[138:139], v[14:15], v[122:123]
	v_pk_mul_f32 v[140:141], v[16:17], v[124:125]
	v_pk_mul_f32 v[142:143], v[18:19], v[126:127]
	v_pk_mul_f32 v[144:145], v[20:21], v[128:129]
	v_pk_mul_f32 v[146:147], v[22:23], v[130:131]
	global_store_dwordx4 v2, v[132:135], s[34:35] offset:0 sc1
	global_store_dwordx4 v2, v[136:139], s[34:35] offset:1024 sc1
	global_store_dwordx4 v2, v[140:143], s[34:35] offset:2048 sc1
	global_store_dwordx4 v2, v[144:147], s[34:35] offset:3072 sc1
	s_branch .Lfin_tail
